# barrier: poll cross-XCD release word directly; layer-0 in-proj GEMM tile order in row-tile pairs (WGM 2)
# speedup vs baseline: 1.0125x; 1.0008x over previous
;     __host__ __device__ bool next(int i, Unit& u) const { const int L = i * G + c; if (L >= nwg) return false; map(L, u); return true; }
; #define PG8_BAR __builtin_amdgcn_s_barrier()
; template <class Epi, class Sched, bool ALIGN_EPI = false, bool SP2 = false, bool F8 = false  >
; __device__ __forceinline__ void gemm_phase(PG8_LAS unsigned char* lds, const Gemm g, const Sched& S, const Epi& E, const int wid_  ) {
;     ...
;     for (int i = 0; i < 2; ++i) { int R, C; stage_rc(tid * 16 + i * 8192, R, C); const int Rb = Epi::PERM ? ((R & ~31) + perm32(R & 31)) : R;
;         voffA[i] = (unsigned)(R * K + C) * 2u; voffB[i] = (unsigned)(Rb * K + C) * 2u; }
;     const unsigned kstep = (unsigned)(BK * 2);
;     const unsigned hstep = (unsigned)HALF * (unsigned)K * 2u;
;     const unsigned tstep = 2u * hstep;
;     const unsigned ldsw = (unsigned)wid * 1024u;
;     const int aoff = lds_byte(wr * 64 + fr, fq * 8), boff = lds_byte(wc * 32 + fr, fq * 8);
;     ...
;     const __amdgpu_buffer_rsrc_t rsrc_voffA = __builtin_amdgcn_make_buffer_rsrc((void*)g.A, 0, 0xFFFFFFFF, 0x00020000), rsrc_voffB = __builtin_amdgcn_make_buffer_rsrc((void*)g.Bt, 0, 0xFFFFFFFF, 0x00020000);
;     ...
;     Unit cur, nxt; int ui = 0;
;     if (!S.next(0, cur)) return;
;     f32x4 acc[2][2][4][2];
; #pragma unroll
;     for (int a = 0; a < 2; ++a)
; #pragma unroll
;         for (int b = 0; b < 2; ++b)
; #pragma unroll
;             for (int m = 0; m < 4; ++m)
; #pragma unroll
;                 for (int n = 0; n < 2; ++n) acc[a][b][m][n] = (f32x4){0.f, 0.f, 0.f, 0.f};
;     bf16x8 At[4][2], B0[2][2], B1[2][2];
;     unsigned cA = (unsigned)cur.pm * tstep, cB = (unsigned)S.b_off(cur, tstep);
;     S.a_ready(cur);
;     if constexpr (SP2) {
;         PG8_STAGE(PG8_SB(0, 0), cB, voffB); PG8_STAGE(PG8_SB(0, 1), cB + hstep, voffB); PG8_STAGE(PG8_SA(0, 0), cA, voffA); PG8_STAGE(PG8_SA(0, 1), cA + hstep, voffA);
;         if (wr == 1) PG8_BAR;
;         PG8_WAIT_V(2); PG8_BAR;
;         PG8_STAGE(PG8_SB(1, 0), cB + kstep, voffB); PG8_STAGE(PG8_SA(1, 0), cA + kstep, voffA); PG8_STAGE(PG8_SB(1, 1), cB + hstep + kstep, voffB);
;         PG8_WAIT_V(6); PG8_BAR;
;     } else {
;         PG8_STAGE(PG8_SB(0, 0), cB, voffB); PG8_STAGE(PG8_SA(0, 0), cA, voffA); PG8_STAGE(PG8_SB(0, 1), cB + hstep, voffB); PG8_STAGE(PG8_SA(0, 1), cA + hstep, voffA);
;         if (wr == 1) PG8_BAR;
;         PG8_WAIT_V(4); PG8_BAR;
.LBB0_221:
	s_and_b64 vcc, exec, s[0:1]
	s_cbranch_vccz .LBB0_237
	s_and_b32 s0, s87, 0xffffffc0
	v_mov_b32_e32 v0, v128
	s_add_u32 s4, s54, 0x800000
	v_add_u32_e32 v1, s0, v0
	v_ashrrev_i32_e32 v3, 31, v1
	v_lshrrev_b32_e32 v3, 26, v3
	s_waitcnt lgkmcnt(0)
	v_readfirstlane_b32 s12, v1
	v_lshlrev_b32_e32 v2, 4, v1
	v_add_u32_e32 v3, v1, v3
	v_bfe_i32 v1, v1, 27, 1
	v_lshrrev_b32_e32 v1, 22, v1
	v_add_u32_e32 v1, v2, v1
	v_and_b32_e32 v1, 0xfffffc00, v1
	v_sub_u32_e32 v1, v2, v1
	v_lshrrev_b32_e32 v4, 4, v1
	v_bitop3_b32 v1, v4, v1, 32 bitop3:0x6c
	v_ashrrev_i32_e32 v5, 31, v1
	v_ashrrev_i32_e32 v3, 6, v3
	v_lshrrev_b32_e32 v5, 26, v5
	v_lshlrev_b32_e32 v4, 3, v3
	v_add_u32_e32 v5, v1, v5
	v_and_b32_e32 v4, -16, v4
	v_ashrrev_i32_e32 v6, 6, v5
	v_and_b32_e32 v5, 0xc0, v5
	v_add_u32_e32 v4, v6, v4
	v_sub_u32_e32 v1, v1, v5
	v_mov_b32_e32 v5, 1
	v_lshlrev_b32_e32 v3, 5, v3
	v_ashrrev_i16_sdwa v1, v5, sext(v1) dst_sel:DWORD dst_unused:UNUSED_PAD src0_sel:DWORD src1_sel:BYTE_0
	v_lshlrev_b32_e32 v7, 1, v4
	v_lshrrev_b32_e32 v8, 2, v4
	v_and_b32_e32 v6, 3, v6
	s_mov_b32 s0, 0xfffe0
	v_and_b32_e32 v3, 32, v3
	v_bfe_i32 v1, v1, 0, 16
	v_and_b32_e32 v7, 24, v7
	v_and_b32_e32 v8, 4, v8
	v_and_or_b32 v6, v4, s0, v6
	v_or3_b32 v6, v6, v8, v7
	v_add_lshl_u32 v1, v3, v1, 1
	v_lshl_add_u32 v129, v4, 12, v1
	v_lshl_add_u32 v130, v6, 12, v1
	v_add_u32_e32 v1, 0x2000, v2
	v_ashrrev_i32_e32 v2, 31, v1
	v_lshrrev_b32_e32 v2, 22, v2
	v_add_u32_e32 v2, v1, v2
	v_ashrrev_i32_e32 v2, 10, v2
	v_mul_i32_i24_e32 v3, 0x400, v2
	v_sub_u32_e32 v1, v1, v3
	v_lshrrev_b32_e32 v3, 4, v1
	v_bitop3_b32 v1, v3, v1, 32 bitop3:0x6c
	s_addc_u32 s1, s55, 0
	v_ashrrev_i32_e32 v4, 31, v1
	v_lshrrev_b32_e32 v4, 26, v4
	s_and_b32 s5, s1, 0xffff
	s_ashr_i32 s1, s2, 31
	v_lshlrev_b32_e32 v3, 3, v2
	v_add_u32_e32 v4, v1, v4
	s_lshr_b32 s1, s1, 29
	v_and_b32_e32 v3, -16, v3
	v_ashrrev_i32_e32 v6, 6, v4
	v_readlane_b32 s6, v254, 55
	s_add_i32 s1, s2, s1
	s_ashr_i32 s13, s12, 6
	v_add_u32_e32 v3, v6, v3
	v_and_b32_e32 v6, 3, v6
	v_readlane_b32 s7, v254, 56
	s_and_b32 s3, s1, -8
	v_and_or_b32 v6, v3, s0, v6
	s_ashr_i32 s30, s12, 8
	s_lshl_b32 s0, s13, 10
	s_and_b32 s93, s7, 0xffff
	s_sub_i32 s6, s2, s3
	s_cmp_lt_i32 s6, 0
	s_movk_i32 s3, 0xe1
	s_cselect_b32 s7, s3, 0xe0
	s_mul_i32 s6, s7, s6
	s_ashr_i32 s1, s1, 3
	s_add_i32 s6, s6, s1
	s_mul_hi_i32 s1, s6, 0x92492493
	s_add_i32 s1, s1, s6
	s_lshr_b32 s7, s1, 31
	s_ashr_i32 s1, s1, 5
	s_add_i32 s1, s1, s7
	s_lshl_b32 s7, s1, 1
	s_mulk_i32 s1, 0x38
	s_sub_i32 s1, s6, s1
	s_sext_i32_i16 s6, s1
	s_bfe_u32 s6, s6, 0x3001c
	v_and_b32_e32 v4, 0xc0, v4
	s_add_i32 s6, s1, s6
	v_sub_u32_e32 v1, v1, v4
	s_sext_i32_i16 s14, s6
	v_lshlrev_b32_e32 v2, 5, v2
	v_ashrrev_i16_sdwa v1, v5, sext(v1) dst_sel:DWORD dst_unused:UNUSED_PAD src0_sel:DWORD src1_sel:BYTE_0
	v_lshlrev_b32_e32 v4, 1, v3
	v_lshrrev_b32_e32 v5, 2, v3
	s_ashr_i32 s39, s14, 1
	s_add_i32 s14, s0, 0
	v_and_b32_e32 v2, 32, v2
	v_bfe_i32 v1, v1, 0, 16
	v_and_b32_e32 v4, 24, v4
	v_and_b32_e32 v5, 4, v5
	s_mov_b32 s95, 0x20000
	s_mov_b32 s94, -1
	s_add_i32 s15, s14, 0x10000
	v_or3_b32 v4, v6, v5, v4
	v_add_lshl_u32 v1, v2, v1, 1
	s_mov_b32 s8, s4
	s_mov_b32 s9, s5
	s_mov_b32 s10, s94
	s_mov_b32 s11, s95
	s_and_b32 s6, s6, 0xfffe
	s_lshl_b32 s60, s39, 20
	s_mov_b32 m0, s15
	s_add_i32 s16, s14, 0x12000
	v_lshl_add_u32 v132, v4, 12, v1
	s_sub_i32 s1, s1, s6
	buffer_load_dwordx4 v130, s[8:11], s60 offen lds
	s_mov_b32 m0, s16
	s_add_i32 s17, s14, 0x14000
	s_sext_i32_i16 s1, s1
	buffer_load_dwordx4 v132, s[8:11], s60 offen lds
	s_or_b32 s0, s60, 0x80000
	s_mov_b32 m0, s17
	s_add_i32 s18, s14, 0x16000
	s_add_i32 s56, s7, s1
	buffer_load_dwordx4 v130, s[8:11], s0 offen lds
	s_mov_b32 m0, s18
	s_lshl_b32 s59, s56, 20
	buffer_load_dwordx4 v132, s[8:11], s0 offen lds
	s_mov_b32 m0, s14
	s_add_i32 s19, s14, 0x2000
	v_lshl_add_u32 v131, v3, 12, v1
	buffer_load_dwordx4 v129, s[92:95], s59 offen lds
	s_mov_b32 m0, s19
	s_add_i32 s20, s14, 0x4000
	buffer_load_dwordx4 v131, s[92:95], s59 offen lds
	s_or_b32 s0, s59, 0x80000
	s_mov_b32 m0, s20
	s_add_i32 s21, s14, 0x6000
	buffer_load_dwordx4 v129, s[92:95], s0 offen lds
	s_mov_b32 m0, s21
	s_cmp_eq_u32 s30, 1
	buffer_load_dwordx4 v131, s[92:95], s0 offen lds
	s_mov_b32 s6, s94
	s_mov_b32 s7, s95
	s_cselect_b64 s[0:1], -1, 0
	s_cmp_lg_u32 s30, 1
	s_mov_b32 s22, 0
	s_cbranch_scc1 .LBB0_224
	s_barrier

;     __host__ __device__ bool next(int i, Unit& u) const { const int L = i * G + c; if (L >= nwg) return false; map(L, u); return true; }
; template <class Epi, class Sched, bool ALIGN_EPI = false, bool SP2 = false, bool F8 = false  >
; __device__ __forceinline__ void gemm_phase(PG8_LAS unsigned char* lds, const Gemm g, const Sched& S, const Epi& E, const int wid_  ) {
;     ...
;         const bool has_next = S.next(ui + 1, nxt);
.LBB0_227:
	s_add_i32 s22, s22, 1
	s_mul_i32 s37, s22, 0x8a
	s_add_i32 s37, s37, s2
	s_cmpk_lt_i32 s37, 0x700
	s_cselect_b64 s[12:13], -1, 0
	s_cmpk_gt_i32 s37, 0x6ff
	s_cbranch_scc1 .LBB0_229
	s_ashr_i32 s35, s37, 31
	s_lshr_b32 s35, s35, 29
	s_add_i32 s35, s37, s35
	s_ashr_i32 s36, s35, 3
	s_and_b32 s35, s35, -8
	s_sub_i32 s35, s37, s35
	s_cmp_lt_i32 s35, 0
	s_cselect_b32 s37, s3, 0xe0
	s_mul_i32 s35, s37, s35
	s_add_i32 s35, s35, s36
	s_mul_hi_i32 s36, s35, 0x92492493
	s_add_i32 s36, s36, s35
	s_lshr_b32 s37, s36, 31
	s_ashr_i32 s36, s36, 5
	s_add_i32 s36, s36, s37
	s_lshl_b32 s37, s36, 1
	s_mulk_i32 s36, 0x38
	s_sub_i32 s35, s35, s36
	s_bfe_u32 s36, s35, 0x3001c
	s_add_i32 s36, s35, s36
	s_sext_i32_i16 s38, s36
	s_and_b32 s36, s36, 0xfffe
	s_sub_i32 s35, s35, s36
	s_sext_i32_i16 s35, s35
	s_add_i32 s36, s37, s35
	s_ashr_i32 s35, s38, 1
